# scan R3: direction loop unrolled with both load sets in flight, layernorm gain/bias loads hoisted, waits recounted by dependence
# baseline (speedup 1.0000x reference)
.LBB0_1981:
	v_add_u32_e32 v36, s20, v31
	v_ashrrev_i32_e32 v37, 31, v36
	v_cndmask_b32_e64 v38, v35, v34, s[14:15]
	v_lshlrev_b64 v[36:37], 20, v[36:37]
	v_cndmask_b32_e64 v18, v47, v46, s[14:15]
	v_lshl_or_b32 v36, v38, 1, v36
	v_lshlrev_b32_e32 v18, 1, v18
	v_lshl_add_u64 v[38:39], s[6:7], 0, v[36:37]
	v_lshl_add_u64 v[40:41], s[94:95], 0, v[36:37]
	v_lshl_add_u64 v[44:45], v[24:25], 0, v[36:37]
	v_lshl_add_u64 v[58:59], v[38:39], 0, v[18:19]
	v_lshl_add_u64 v[60:61], v[40:41], 0, v[18:19]
	global_load_dwordx4 v[36:39], v[44:45], off
	global_load_dwordx4 v[40:43], v[44:45], off offset:64
	global_load_dwordx4 v[50:53], v[44:45], off offset:2048
	global_load_dwordx4 v[54:57], v[44:45], off offset:2112
	v_add_co_u32_e32 v44, vcc, s17, v44
	v_lshl_add_u64 v[78:79], v[58:59], 0, v[26:27]
	s_nop 0
	v_addc_co_u32_e32 v45, vcc, 0, v45, vcc
	v_lshl_add_u64 v[82:83], v[60:61], 0, v[28:29]
	global_load_dwordx4 v[58:61], v[44:45], off
	global_load_dwordx4 v[62:65], v[44:45], off offset:64
	global_load_dwordx4 v[66:69], v[44:45], off offset:2048
	global_load_dwordx4 v[70:73], v[44:45], off offset:2112
	global_load_dwordx4 v[74:77], v[78:79], off
	s_nop 0
	global_load_dwordx2 v[44:45], v[82:83], off
	global_load_dwordx2 v[84:85], v[82:83], off offset:32
	s_nop 0
	global_load_dwordx4 v[78:81], v[78:79], off offset:64
	s_nop 0
	global_load_dwordx2 v[86:87], v[82:83], off offset:64
	s_nop 0
	global_load_dwordx2 v[82:83], v[82:83], off offset:96
	s_mov_b32 s20, 16
	s_mov_b64 s[14:15], 0
	v_mov_b32_e32 v119, 0
	v_add_u32_e32 v136, s20, v31
	v_ashrrev_i32_e32 v137, 31, v136
	v_cndmask_b32_e64 v138, v35, v34, s[14:15]
	v_lshlrev_b64 v[136:137], 20, v[136:137]
	v_cndmask_b32_e64 v118, v47, v46, s[14:15]
	v_lshl_or_b32 v136, v138, 1, v136
	v_lshlrev_b32_e32 v118, 1, v118
	v_lshl_add_u64 v[138:139], s[6:7], 0, v[136:137]
	v_lshl_add_u64 v[140:141], s[94:95], 0, v[136:137]
	v_lshl_add_u64 v[144:145], v[24:25], 0, v[136:137]
	v_lshl_add_u64 v[158:159], v[138:139], 0, v[118:119]
	v_lshl_add_u64 v[160:161], v[140:141], 0, v[118:119]
	global_load_dwordx4 v[136:139], v[144:145], off
	global_load_dwordx4 v[140:143], v[144:145], off offset:64
	global_load_dwordx4 v[150:153], v[144:145], off offset:2048
	global_load_dwordx4 v[154:157], v[144:145], off offset:2112
	v_add_co_u32_e32 v144, vcc, s17, v144
	v_lshl_add_u64 v[178:179], v[158:159], 0, v[26:27]
	s_nop 0
	v_addc_co_u32_e32 v145, vcc, 0, v145, vcc
	v_lshl_add_u64 v[182:183], v[160:161], 0, v[28:29]
	global_load_dwordx4 v[158:161], v[144:145], off
	global_load_dwordx4 v[162:165], v[144:145], off offset:64
	global_load_dwordx4 v[166:169], v[144:145], off offset:2048
	global_load_dwordx4 v[170:173], v[144:145], off offset:2112
	global_load_dwordx4 v[174:177], v[178:179], off
	s_nop 0
	global_load_dwordx2 v[144:145], v[182:183], off
	global_load_dwordx2 v[184:185], v[182:183], off offset:32
	s_nop 0
	global_load_dwordx4 v[178:181], v[178:179], off offset:64
	s_nop 0
	global_load_dwordx2 v[186:187], v[182:183], off offset:64
	s_nop 0
	global_load_dwordx2 v[182:183], v[182:183], off offset:96
	s_waitcnt vmcnt(19)
	v_mfma_f32_16x16x32_bf16 v[10:13], v[36:39], v[74:77], v[10:13]
	s_waitcnt vmcnt(18)
	v_lshlrev_b32_e32 v36, 16, v44
	v_and_b32_e32 v37, 0xffff0000, v44
	v_lshlrev_b32_e32 v38, 16, v45
	v_mfma_f32_16x16x32_bf16 v[6:9], v[50:53], v[74:77], v[6:9]
	v_and_b32_e32 v39, 0xffff0000, v45
	s_waitcnt vmcnt(17)
	v_lshlrev_b32_e32 v44, 16, v84
	v_and_b32_e32 v45, 0xffff0000, v84
	v_mfma_f32_16x16x32_bf16 v[2:5], v[58:61], v[74:77], v[2:5]
	v_lshlrev_b32_e32 v50, 16, v85
	v_and_b32_e32 v51, 0xffff0000, v85
	s_waitcnt vmcnt(14)
	v_lshlrev_b32_e32 v52, 16, v82
	v_mfma_f32_16x16x32_bf16 v[14:17], v[66:69], v[74:77], v[14:17]
	v_and_b32_e32 v53, 0xffff0000, v82
	v_mfma_f32_16x16x32_bf16 v[10:13], v[40:43], v[78:81], v[10:13]
	v_lshlrev_b32_e32 v40, 16, v86
	v_and_b32_e32 v41, 0xffff0000, v86
	v_lshlrev_b32_e32 v42, 16, v87
	v_mfma_f32_16x16x32_bf16 v[6:9], v[54:57], v[78:81], v[6:9]
	v_and_b32_e32 v43, 0xffff0000, v87
	v_lshlrev_b32_e32 v54, 16, v83
	v_and_b32_e32 v55, 0xffff0000, v83
	v_mfma_f32_16x16x32_bf16 v[2:5], v[62:65], v[78:81], v[2:5]
	v_add_f32_e64 v12, v12, v38
	v_add_f32_e64 v13, v13, v39
	v_pk_add_f32 v[10:11], v[10:11], v[36:37]
	s_nop 0
	v_pk_add_f32 v[8:9], v[8:9], v[50:51]
	v_mfma_f32_16x16x32_bf16 v[14:17], v[70:73], v[78:81], v[14:17]
	v_add_f32_e64 v6, v6, v44
	v_add_f32_e64 v7, v7, v45
	v_pk_add_f32 v[4:5], v[4:5], v[42:43]
	v_pk_add_f32 v[2:3], v[2:3], v[40:41]
	s_nop 3
	v_pk_add_f32 v[16:17], v[16:17], v[54:55]
	v_pk_add_f32 v[14:15], v[14:15], v[52:53]
	s_waitcnt vmcnt(5)
	v_mfma_f32_16x16x32_bf16 v[10:13], v[136:139], v[174:177], v[10:13]
	s_waitcnt vmcnt(4)
	v_lshlrev_b32_e32 v136, 16, v144
	v_and_b32_e32 v137, 0xffff0000, v144
	v_lshlrev_b32_e32 v138, 16, v145
	v_mfma_f32_16x16x32_bf16 v[6:9], v[150:153], v[174:177], v[6:9]
	v_and_b32_e32 v139, 0xffff0000, v145
	s_waitcnt vmcnt(3)
	v_lshlrev_b32_e32 v144, 16, v184
	v_and_b32_e32 v145, 0xffff0000, v184
	v_mfma_f32_16x16x32_bf16 v[2:5], v[158:161], v[174:177], v[2:5]
	v_lshlrev_b32_e32 v150, 16, v185
	v_and_b32_e32 v151, 0xffff0000, v185
	s_waitcnt vmcnt(0)
	v_lshlrev_b32_e32 v152, 16, v182
	v_mfma_f32_16x16x32_bf16 v[14:17], v[166:169], v[174:177], v[14:17]
	v_and_b32_e32 v153, 0xffff0000, v182
	v_mfma_f32_16x16x32_bf16 v[10:13], v[140:143], v[178:181], v[10:13]
	v_lshlrev_b32_e32 v140, 16, v186
	v_and_b32_e32 v141, 0xffff0000, v186
	v_lshlrev_b32_e32 v142, 16, v187
	v_mfma_f32_16x16x32_bf16 v[6:9], v[154:157], v[178:181], v[6:9]
	v_and_b32_e32 v143, 0xffff0000, v187
	v_lshlrev_b32_e32 v154, 16, v183
	v_and_b32_e32 v155, 0xffff0000, v183
	v_mfma_f32_16x16x32_bf16 v[2:5], v[162:165], v[178:181], v[2:5]
	v_add_f32_e64 v12, v12, v138
	v_add_f32_e64 v13, v13, v139
	v_pk_add_f32 v[10:11], v[10:11], v[136:137]
	s_nop 0
	v_pk_add_f32 v[8:9], v[8:9], v[150:151]
	v_mfma_f32_16x16x32_bf16 v[14:17], v[170:173], v[178:181], v[14:17]
	v_add_f32_e64 v6, v6, v144
	v_add_f32_e64 v7, v7, v145
	v_pk_add_f32 v[4:5], v[4:5], v[142:143]
	v_pk_add_f32 v[2:3], v[2:3], v[140:141]
	s_nop 3
	v_pk_add_f32 v[16:17], v[16:17], v[154:155]
	v_pk_add_f32 v[14:15], v[14:15], v[152:153]
	v_ashrrev_i32_e32 v31, 31, v30
	v_lshlrev_b64 v[34:35], 13, v[30:31]
	v_lshl_or_b32 v18, v33, 6, v34
	v_or_b32_e32 v34, v18, v22
	v_lshlrev_b64 v[36:37], 10, v[34:35]
	v_lshl_or_b32 v44, v32, 6, v20
	v_lshlrev_b64 v[30:31], 11, v[34:35]
	v_lshl_add_u64 v[34:35], s[92:93], 0, v[36:37]
	v_lshl_add_u64 v[32:33], s[2:3], 0, v[30:31]
	v_lshlrev_b32_e32 v18, 1, v44
	v_lshl_add_u64 v[38:39], s[8:9], 0, v[36:37]
	v_lshl_add_u64 v[40:41], v[34:35], 0, s[12:13]
	v_lshl_add_u64 v[32:33], v[32:33], 0, v[18:19]
	v_lshl_add_u64 v[76:77], v[34:35], 0, v[18:19]
	v_lshl_add_u64 v[42:43], v[38:39], 0, v[18:19]
	v_lshl_add_u64 v[34:35], v[40:41], 0, v[18:19]
	global_load_dwordx2 v[74:75], v[32:33], off
	global_load_dwordx2 v[78:79], v[76:77], off
	global_load_dwordx2 v[80:81], v[42:43], off
	global_load_dwordx2 v[82:83], v[34:35], off
	v_readlane_b32 s52, v253, 45
	v_lshlrev_b32_e32 v49, 2, v44
	v_readlane_b32 s58, v253, 51
	v_readlane_b32 s59, v253, 52
	v_readlane_b32 s60, v253, 53
	v_readlane_b32 s61, v253, 54
	v_readlane_b32 s62, v253, 55
	v_readlane_b32 s63, v253, 56
	v_readlane_b32 s64, v253, 57
	v_readlane_b32 s65, v253, 58
	s_mov_b64 s[24:25], s[60:61]
	global_load_dwordx4 v[50:53], v49, s[58:59]
	global_load_dwordx4 v[54:57], v49, s[24:25]
	v_mov_b32_e32 v34, v11
	v_mov_b32_e32 v35, v12
	v_mov_b32_e32 v58, v10
	v_mov_b32_e32 v59, v13
	v_mov_b32_e32 v60, v7
	v_mov_b32_e32 v61, v8
	v_mov_b32_e32 v62, v6
	v_mov_b32_e32 v63, v9
	v_pk_add_f32 v[34:35], v[34:35], v[58:59]
	v_pk_add_f32 v[58:59], v[60:61], v[62:63]
	v_add_f32_e32 v84, v34, v35
	v_pk_add_f32 v[34:35], v[58:59], v[58:59] op_sel:[0,1] op_sel_hi:[1,0]
	v_add_f32_e32 v64, v2, v3
	v_add_f32_e32 v66, v4, v5
	v_mov_b32_e32 v85, v14
	v_mov_b32_e32 v65, v16
	v_mov_b32_e32 v67, v17
	v_mov_b32_e32 v69, v19
	v_or_b32_e32 v68, 32, v18
	v_add_f32_e32 v84, 0, v84
	v_mov_b32_e32 v35, v15
	v_pk_add_f32 v[90:91], v[64:65], v[66:67]
	v_lshl_add_u64 v[60:61], v[40:41], 0, v[68:69]
	v_pk_add_f32 v[34:35], v[84:85], v[34:35]
	global_load_dwordx2 v[38:39], v[32:33], off offset:32
	global_load_dwordx2 v[44:45], v[42:43], off offset:32
	global_load_dwordx2 v[88:89], v[76:77], off offset:32
	global_load_dwordx2 v[92:93], v[60:61], off
	v_pk_add_f32 v[34:35], v[34:35], v[90:91]
	global_load_dwordx4 v[58:61], v49, s[24:25] offset:64
	global_load_dwordx4 v[62:65], v49, s[58:59] offset:64
	v_add_f32_e32 v94, v34, v35
	ds_bpermute_b32 v95, v21, v94
	v_mov_b32_e32 v87, v19
	v_or_b32_e32 v86, 64, v18
	v_lshl_add_u64 v[84:85], v[40:41], 0, v[86:87]
	global_load_dwordx4 v[66:69], v49, s[24:25] offset:128
	global_load_dwordx4 v[70:73], v49, s[58:59] offset:128
	s_waitcnt lgkmcnt(0)
	v_add_f32_e32 v98, v94, v95
	ds_bpermute_b32 v99, v23, v98
	global_load_dwordx2 v[34:35], v[32:33], off offset:1024
	global_load_dwordx2 v[86:87], v[32:33], off offset:64
	global_load_dwordx2 v[90:91], v[32:33], off offset:96
	global_load_dwordx2 v[94:95], v[76:77], off offset:64
	s_nop 0
	global_load_dwordx2 v[76:77], v[76:77], off offset:96
	s_nop 0
	global_load_dwordx2 v[84:85], v[84:85], off
	s_nop 0
	global_load_dwordx2 v[96:97], v[42:43], off offset:64
	v_lshl_add_u64 v[36:37], s[68:69], 0, v[36:37]
	s_waitcnt lgkmcnt(0)
	v_add_f32_e32 v98, v98, v99
	s_mov_b64 s[26:27], s[62:63]
	v_lshl_add_u64 v[36:37], v[36:37], 0, v[18:19]
	s_mov_b64 s[28:29], s[64:65]
	v_add_u32_e32 v1, s16, v1
	v_readlane_b32 s53, v253, 46
	v_readlane_b32 s54, v253, 47
	v_readlane_b32 s55, v253, 48
	v_readlane_b32 s56, v253, 49
	v_readlane_b32 s57, v253, 50
	v_readlane_b32 s66, v253, 59
	v_readlane_b32 s67, v253, 60
	s_waitcnt vmcnt(20)
	v_lshlrev_b32_e32 v99, 16, v74
	s_waitcnt vmcnt(19)
	v_lshlrev_b32_e32 v101, 16, v78
	v_lshlrev_b32_e32 v102, 16, v79
	s_waitcnt vmcnt(17)
	v_lshlrev_b32_e32 v105, 16, v82
	v_and_b32_e32 v79, 0xffff0000, v79
	v_lshlrev_b32_e32 v103, 16, v80
	v_lshlrev_b32_e32 v106, 16, v83
	v_and_b32_e32 v83, 0xffff0000, v83
	v_add_f32_e32 v101, v101, v105
	v_add_f32_e32 v79, v79, v83
	v_mul_f32_e32 v83, v99, v103
	v_add_f32_e32 v99, -2.0, v101
	v_and_b32_e32 v78, 0xffff0000, v78
	v_and_b32_e32 v82, 0xffff0000, v82
	s_waitcnt vmcnt(16)
	v_fma_f32 v50, v50, v99, 2.0
	v_add_f32_e32 v78, v78, v82
	v_mul_f32_e32 v50, v83, v50
	v_and_b32_e32 v74, 0xffff0000, v74
	v_and_b32_e32 v80, 0xffff0000, v80
	s_waitcnt vmcnt(15)
	v_fma_f32 v83, v54, v50, 0
	v_add_f32_e32 v54, -2.0, v78
	v_add_f32_e32 v82, v102, v106
	v_mul_f32_e32 v50, v74, v80
	v_fma_f32 v51, v51, v54, 2.0
	v_lshlrev_b32_e32 v100, 16, v75
	v_lshlrev_b32_e32 v104, 16, v81
	v_mul_f32_e32 v50, v50, v51
	v_add_f32_e32 v51, -2.0, v82
	v_fmac_f32_e32 v83, v55, v50
	v_mul_f32_e32 v50, v100, v104
	v_fma_f32 v51, v52, v51, 2.0
	v_and_b32_e32 v75, 0xffff0000, v75
	v_and_b32_e32 v81, 0xffff0000, v81
	v_mul_f32_e32 v50, v50, v51
	v_fmac_f32_e32 v83, v56, v50
	v_mul_f32_e32 v50, v75, v81
	global_load_dwordx2 v[74:75], v[42:43], off offset:96
	v_or_b32_e32 v42, 0x60, v18
	v_mov_b32_e32 v43, v19
	v_lshl_add_u64 v[40:41], v[40:41], 0, v[42:43]
	v_add_f32_e32 v51, -2.0, v79
	global_load_dwordx2 v[78:79], v[40:41], off
	v_fma_f32 v51, v53, v51, 2.0
	v_mul_f32_e32 v50, v50, v51
	v_fmac_f32_e32 v83, v57, v50
	global_load_dwordx4 v[40:43], v49, s[24:25] offset:192
	global_load_dwordx4 v[50:53], v49, s[58:59] offset:192
	s_waitcnt vmcnt(16)
	v_lshlrev_b32_e32 v56, 16, v88
	s_waitcnt vmcnt(15)
	v_lshlrev_b32_e32 v57, 16, v92
	v_lshlrev_b32_e32 v54, 16, v38
	v_lshlrev_b32_e32 v55, 16, v44
	v_add_f32_e32 v56, v56, v57
	v_and_b32_e32 v57, 0xffff0000, v88
	v_and_b32_e32 v82, 0xffff0000, v92
	v_and_b32_e32 v38, 0xffff0000, v38
	v_and_b32_e32 v44, 0xffff0000, v44
	v_add_f32_e32 v57, v57, v82
	v_mul_f32_e32 v54, v54, v55
	v_add_f32_e32 v55, -2.0, v56
	s_waitcnt vmcnt(13)
	v_fma_f32 v55, v62, v55, 2.0
	v_mul_f32_e32 v38, v38, v44
	v_add_f32_e32 v44, -2.0, v57
	v_mul_f32_e32 v54, v54, v55
	v_fma_f32 v44, v63, v44, 2.0
	v_fmac_f32_e32 v83, v58, v54
	v_mul_f32_e32 v38, v38, v44
	v_fmac_f32_e32 v83, v59, v38
	v_and_b32_e32 v55, 0xffff0000, v39
	v_lshlrev_b32_e32 v54, 16, v39
	v_and_b32_e32 v39, 0xffff0000, v45
	v_lshlrev_b32_e32 v38, 16, v45
	v_and_b32_e32 v45, 0xffff0000, v89
	v_lshlrev_b32_e32 v44, 16, v89
	v_and_b32_e32 v57, 0xffff0000, v93
	v_lshlrev_b32_e32 v56, 16, v93
	v_pk_add_f32 v[44:45], v[44:45], v[56:57]
	v_pk_mul_f32 v[38:39], v[54:55], v[38:39]
	v_pk_add_f32 v[44:45], v[44:45], -2.0 op_sel_hi:[1,0]
	s_waitcnt vmcnt(7)
	v_and_b32_e32 v55, 0xffff0000, v94
	v_pk_fma_f32 v[44:45], v[64:65], v[44:45], 2.0 op_sel_hi:[1,1,0]
	v_lshlrev_b32_e32 v54, 16, v94
	v_pk_mul_f32 v[38:39], v[38:39], v[44:45]
	s_waitcnt vmcnt(5)
	v_and_b32_e32 v57, 0xffff0000, v84
	v_pk_mul_f32 v[38:39], v[60:61], v[38:39]
	v_lshlrev_b32_e32 v56, 16, v84
	v_add_f32_e32 v38, v38, v83
	v_add_f32_e32 v58, v39, v38
	v_and_b32_e32 v39, 0xffff0000, v86
	v_lshlrev_b32_e32 v38, 16, v86
	s_waitcnt vmcnt(4)
	v_and_b32_e32 v45, 0xffff0000, v96
	v_lshlrev_b32_e32 v44, 16, v96
	v_pk_add_f32 v[54:55], v[54:55], v[56:57]
	v_pk_mul_f32 v[38:39], v[38:39], v[44:45]
	v_pk_add_f32 v[44:45], v[54:55], -2.0 op_sel_hi:[1,0]
	v_and_b32_e32 v55, 0xffff0000, v95
	v_pk_fma_f32 v[44:45], v[70:71], v[44:45], 2.0 op_sel_hi:[1,1,0]
	v_lshlrev_b32_e32 v54, 16, v95
	v_pk_mul_f32 v[38:39], v[38:39], v[44:45]
	v_and_b32_e32 v57, 0xffff0000, v85
	v_pk_mul_f32 v[38:39], v[66:67], v[38:39]
	v_lshlrev_b32_e32 v56, 16, v85
	v_add_f32_e32 v38, v58, v38
	v_add_f32_e32 v58, v39, v38
	v_and_b32_e32 v39, 0xffff0000, v87
	v_lshlrev_b32_e32 v38, 16, v87
	v_and_b32_e32 v45, 0xffff0000, v97
	v_lshlrev_b32_e32 v44, 16, v97
	v_pk_add_f32 v[54:55], v[54:55], v[56:57]
	v_pk_mul_f32 v[38:39], v[38:39], v[44:45]
	v_pk_add_f32 v[44:45], v[54:55], -2.0 op_sel_hi:[1,0]
	v_and_b32_e32 v55, 0xffff0000, v76
	v_pk_fma_f32 v[44:45], v[72:73], v[44:45], 2.0 op_sel_hi:[1,1,0]
	v_lshlrev_b32_e32 v54, 16, v76
	v_pk_mul_f32 v[38:39], v[38:39], v[44:45]
	global_load_dwordx2 v[80:81], v[36:37], off
	v_pk_mul_f32 v[38:39], v[68:69], v[38:39]
	v_and_b32_e32 v59, 0xffff0000, v77
	v_add_f32_e32 v38, v38, v58
	v_add_f32_e32 v58, v39, v38
	v_and_b32_e32 v39, 0xffff0000, v90
	v_lshlrev_b32_e32 v38, 16, v90
	s_waitcnt vmcnt(4)
	v_and_b32_e32 v45, 0xffff0000, v74
	s_waitcnt vmcnt(3)
	v_and_b32_e32 v57, 0xffff0000, v78
	v_lshlrev_b32_e32 v56, 16, v78
	v_lshlrev_b32_e32 v44, 16, v74
	v_pk_add_f32 v[54:55], v[54:55], v[56:57]
	v_pk_mul_f32 v[38:39], v[38:39], v[44:45]
	v_pk_add_f32 v[44:45], v[54:55], -2.0 op_sel_hi:[1,0]
	v_and_b32_e32 v61, 0xffff0000, v79
	s_waitcnt vmcnt(1)
	v_pk_fma_f32 v[44:45], v[50:51], v[44:45], 2.0 op_sel_hi:[1,1,0]
	v_lshlrev_b32_e32 v60, 16, v79
	v_pk_mul_f32 v[38:39], v[38:39], v[44:45]
	v_and_b32_e32 v51, 0xffff0000, v75
	v_pk_mul_f32 v[44:45], v[40:41], v[38:39]
	global_load_dwordx4 v[38:41], v49, s[26:27]
	global_load_dwordx4 v[54:57], v49, s[28:29]
	global_load_dwordx4 v[210:213], v49, s[26:27] offset:64
	global_load_dwordx4 v[214:217], v49, s[28:29] offset:64
	global_load_dwordx4 v[218:221], v49, s[26:27] offset:128
	global_load_dwordx4 v[222:225], v49, s[28:29] offset:128
	global_load_dwordx4 v[226:229], v49, s[26:27] offset:192
	global_load_dwordx4 v[230:233], v49, s[28:29] offset:192
	v_add_f32_e32 v44, v58, v44
	v_lshlrev_b32_e32 v58, 16, v77
	v_add_f32_e32 v62, v45, v44
	v_and_b32_e32 v45, 0xffff0000, v91
	v_lshlrev_b32_e32 v44, 16, v91
	v_lshlrev_b32_e32 v50, 16, v75
	v_pk_add_f32 v[58:59], v[58:59], v[60:61]
	v_pk_mul_f32 v[44:45], v[44:45], v[50:51]
	v_pk_add_f32 v[50:51], v[58:59], -2.0 op_sel_hi:[1,0]
	global_load_dwordx2 v[58:59], v[32:33], off offset:1056
	global_load_dwordx2 v[60:61], v[32:33], off offset:1088
	s_nop 0
	global_load_dwordx2 v[32:33], v[32:33], off offset:1120
	v_pk_fma_f32 v[50:51], v[52:53], v[50:51], 2.0 op_sel_hi:[1,1,0]
	s_nop 0
	v_pk_mul_f32 v[44:45], v[44:45], v[50:51]
	s_nop 0
	v_pk_mul_f32 v[42:43], v[42:43], v[44:45]
	s_nop 0
	v_add_f32_e32 v42, v42, v62
	v_add_f32_e32 v43, v43, v42
	ds_bpermute_b32 v52, v21, v43
	v_mul_f32_e32 v42, 0x3c800000, v98
	v_pk_add_f32 v[44:45], v[14:15], v[42:43] op_sel_hi:[1,0] neg_lo:[0,1] neg_hi:[0,1]
	v_pk_add_f32 v[10:11], v[10:11], v[42:43] op_sel_hi:[1,0] neg_lo:[0,1] neg_hi:[0,1]
	v_pk_add_f32 v[12:13], v[12:13], v[42:43] op_sel_hi:[1,0] neg_lo:[0,1] neg_hi:[0,1]
	s_waitcnt lgkmcnt(0)
	v_add_f32_e32 v14, v43, v52
	ds_bpermute_b32 v15, v23, v14
	v_pk_mul_f32 v[64:65], v[10:11], v[10:11]
	v_pk_mul_f32 v[62:63], v[12:13], v[12:13]
	v_pk_add_f32 v[68:69], v[6:7], v[42:43] op_sel_hi:[1,0] neg_lo:[0,1] neg_hi:[0,1]
	v_pk_add_f32 v[66:67], v[8:9], v[42:43] op_sel_hi:[1,0] neg_lo:[0,1] neg_hi:[0,1]
	s_waitcnt lgkmcnt(0)
	v_add_f32_e32 v14, v14, v15
	v_add_f32_e32 v15, v64, v65
	v_add_f32_e32 v15, v62, v15
	v_pk_mul_f32 v[6:7], v[68:69], v[68:69]
	v_add_f32_e32 v15, v63, v15
	v_add_f32_e32 v6, v6, v15
	v_pk_mul_f32 v[8:9], v[66:67], v[66:67]
	v_add_f32_e32 v6, v7, v6
	v_pk_add_f32 v[16:17], v[16:17], v[42:43] op_sel_hi:[1,0] neg_lo:[0,1] neg_hi:[0,1]
	v_pk_add_f32 v[70:71], v[4:5], v[42:43] op_sel_hi:[1,0] neg_lo:[0,1] neg_hi:[0,1]
	v_pk_add_f32 v[42:43], v[2:3], v[42:43] op_sel_hi:[1,0] neg_lo:[0,1] neg_hi:[0,1]
	v_add_f32_e32 v6, v8, v6
	v_pk_mul_f32 v[2:3], v[42:43], v[42:43]
	v_add_f32_e32 v6, v9, v6
	v_add_f32_e32 v2, v2, v6
	v_pk_mul_f32 v[4:5], v[70:71], v[70:71]
	v_add_f32_e32 v2, v3, v2
	v_add_f32_e32 v2, v4, v2
	v_pk_mul_f32 v[50:51], v[44:45], v[44:45]
	v_add_f32_e32 v2, v5, v2
	v_add_f32_e32 v2, v50, v2
	v_pk_mul_f32 v[52:53], v[16:17], v[16:17]
	v_add_f32_e32 v2, v51, v2
	v_add_f32_e32 v2, v52, v2
	v_add_f32_e32 v7, v53, v2
	ds_bpermute_b32 v8, v21, v7
	v_lshl_add_u64 v[2:3], s[88:89], 0, v[30:31]
	v_lshlrev_b32_e32 v4, 16, v35
	v_and_b32_e32 v5, 0xffff0000, v35
	v_and_b32_e32 v9, 0xffff0000, v34
	s_waitcnt lgkmcnt(0)
	v_add_f32_e32 v15, v7, v8
	ds_bpermute_b32 v31, v23, v15
	v_lshlrev_b32_e32 v8, 16, v34
	v_lshl_add_u64 v[34:35], v[2:3], 0, v[18:19]
	s_waitcnt vmcnt(11)
	v_lshlrev_b32_e32 v6, 16, v81
	v_and_b32_e32 v7, 0xffff0000, v81
	s_waitcnt lgkmcnt(0)
	v_add_f32_e32 v15, v15, v31
	v_fmamk_f32 v15, v15, 0x3c800000, v48
	v_mul_f32_e32 v31, 0x4b800000, v15
	v_cmp_gt_f32_e32 vcc, s18, v15
	v_lshlrev_b32_e32 v30, 16, v80
	global_load_dwordx2 v[50:51], v[36:37], off offset:32
	v_cndmask_b32_e32 v15, v15, v31, vcc
	v_rsq_f32_e32 v15, v15
	v_and_b32_e32 v31, 0xffff0000, v80
	v_mul_f32_e32 v2, 0x45800000, v15
	v_cndmask_b32_e32 v18, v15, v2, vcc
	v_pk_mul_f32 v[2:3], v[10:11], v[18:19] op_sel_hi:[1,0]
	v_cmp_lt_i32_e32 vcc, s19, v1
	s_waitcnt vmcnt(10)
	v_pk_fma_f32 v[2:3], v[2:3], v[38:39], v[54:55]
	s_or_b64 s[10:11], vcc, s[10:11]
	v_pk_fma_f32 v[2:3], v[14:15], v[8:9], v[2:3] op_sel_hi:[0,1,1]
	v_pk_mul_f32 v[8:9], v[12:13], v[18:19] op_sel_hi:[1,0]
	v_pk_mul_f32 v[2:3], v[2:3], v[30:31]
	v_pk_fma_f32 v[8:9], v[8:9], v[40:41], v[56:57]
	v_cvt_pk_bf16_f32 v2, v2, v3
	v_pk_fma_f32 v[4:5], v[14:15], v[4:5], v[8:9] op_sel_hi:[0,1,1]
	v_pk_mul_f32 v[4:5], v[4:5], v[6:7]
	s_waitcnt vmcnt(3)
	v_lshlrev_b32_e32 v10, 16, v59
	v_cvt_pk_bf16_f32 v3, v4, v5
	global_store_dwordx2 v[34:35], v[2:3], off offset:1024
	s_nop 0
	global_load_dwordx2 v[12:13], v[36:37], off offset:64
	global_load_dwordx2 v[30:31], v[36:37], off offset:96
	v_and_b32_e32 v11, 0xffff0000, v59
	v_lshlrev_b32_e32 v38, 16, v58
	v_and_b32_e32 v39, 0xffff0000, v58
	s_waitcnt vmcnt(3)
	v_lshlrev_b32_e32 v36, 16, v51
	v_and_b32_e32 v37, 0xffff0000, v51
	v_lshlrev_b32_e32 v40, 16, v50
	v_and_b32_e32 v41, 0xffff0000, v50
	v_pk_mul_f32 v[50:51], v[68:69], v[18:19] op_sel_hi:[1,0]
	s_waitcnt vmcnt(3)
	v_pk_fma_f32 v[2:3], v[50:51], v[210:211], v[214:215]
	v_pk_mul_f32 v[6:7], v[66:67], v[18:19] op_sel_hi:[1,0]
	v_pk_fma_f32 v[2:3], v[14:15], v[38:39], v[2:3] op_sel_hi:[0,1,1]
	v_pk_fma_f32 v[4:5], v[6:7], v[212:213], v[216:217]
	v_pk_mul_f32 v[2:3], v[2:3], v[40:41]
	v_pk_fma_f32 v[4:5], v[14:15], v[10:11], v[4:5] op_sel_hi:[0,1,1]
	v_pk_mul_f32 v[4:5], v[4:5], v[36:37]
	v_cvt_pk_bf16_f32 v2, v2, v3
	v_cvt_pk_bf16_f32 v3, v4, v5
	global_store_dwordx2 v[34:35], v[2:3], off offset:1056
	s_nop 0
	s_waitcnt vmcnt(2)
	v_lshlrev_b32_e32 v36, 16, v13
	v_and_b32_e32 v37, 0xffff0000, v13
	v_lshlrev_b32_e32 v40, 16, v12
	v_and_b32_e32 v41, 0xffff0000, v12
	v_pk_mul_f32 v[12:13], v[42:43], v[18:19] op_sel_hi:[1,0]
	v_lshlrev_b32_e32 v10, 16, v61
	v_and_b32_e32 v11, 0xffff0000, v61
	v_lshlrev_b32_e32 v38, 16, v60
	v_and_b32_e32 v39, 0xffff0000, v60
	s_waitcnt vmcnt(1)
	v_pk_fma_f32 v[2:3], v[12:13], v[218:219], v[222:223]
	v_pk_mul_f32 v[6:7], v[70:71], v[18:19] op_sel_hi:[1,0]
	v_pk_fma_f32 v[2:3], v[14:15], v[38:39], v[2:3] op_sel_hi:[0,1,1]
	v_pk_fma_f32 v[4:5], v[6:7], v[220:221], v[224:225]
	v_pk_mul_f32 v[2:3], v[2:3], v[40:41]
	v_pk_fma_f32 v[4:5], v[14:15], v[10:11], v[4:5] op_sel_hi:[0,1,1]
	v_pk_mul_f32 v[4:5], v[4:5], v[36:37]
	v_cvt_pk_bf16_f32 v2, v2, v3
	v_cvt_pk_bf16_f32 v3, v4, v5
	global_store_dwordx2 v[34:35], v[2:3], off offset:1088
	s_nop 0
	v_pk_mul_f32 v[10:11], v[44:45], v[18:19] op_sel_hi:[1,0]
	v_pk_mul_f32 v[12:13], v[16:17], v[18:19] op_sel_hi:[1,0]
	v_lshlrev_b32_e32 v16, 16, v32
	v_and_b32_e32 v17, 0xffff0000, v32
	v_lshlrev_b32_e32 v32, 16, v33
	v_and_b32_e32 v33, 0xffff0000, v33
	v_lshlrev_b32_e32 v36, 16, v30
	v_and_b32_e32 v37, 0xffff0000, v30
	v_lshlrev_b32_e32 v30, 16, v31
	v_and_b32_e32 v31, 0xffff0000, v31
	s_waitcnt vmcnt(2)
	v_pk_fma_f32 v[2:3], v[10:11], v[226:227], v[230:231]
	v_pk_fma_f32 v[4:5], v[12:13], v[228:229], v[232:233]
	v_pk_fma_f32 v[2:3], v[14:15], v[16:17], v[2:3] op_sel_hi:[0,1,1]
	v_pk_fma_f32 v[4:5], v[14:15], v[32:33], v[4:5] op_sel_hi:[0,1,1]
	v_pk_mul_f32 v[2:3], v[2:3], v[36:37]
	v_pk_mul_f32 v[4:5], v[4:5], v[30:31]
	v_cvt_pk_bf16_f32 v2, v2, v3
	v_cvt_pk_bf16_f32 v3, v4, v5
	global_store_dwordx2 v[34:35], v[2:3], off offset:1120
	s_andn2_b64 exec, exec, s[10:11]
	s_cbranch_execnz .LBB0_1980
